# v5 attention: serpentine q-block order so consecutive MFMAs share one operand
# speedup vs baseline: 1.0278x; 1.0099x over previous
.LBB0_733:
	s_or_b64 exec, exec, s[8:9]
	s_movk_i32 s4, 0xf0
	s_cmp_lg_u32 0, -1
	v_lshlrev_b32_e32 v39, 8, v141
	v_bitop3_b32 v80, v142, s4, v136 bitop3:0x48
	s_cselect_b32 s10, 0, 0
	v_cvt_pk_bf16_f32 v96, v134, v135
	v_cvt_pk_bf16_f32 v97, v132, v133
	v_cvt_pk_bf16_f32 v98, v130, v131
	v_cvt_pk_bf16_f32 v99, v128, v129
	v_cvt_pk_bf16_f32 v100, v126, v127
	v_cvt_pk_bf16_f32 v101, v124, v125
	v_cvt_pk_bf16_f32 v102, v122, v123
	v_cvt_pk_bf16_f32 v103, v120, v121
	v_cvt_pk_bf16_f32 v104, v70, v71
	v_cvt_pk_bf16_f32 v105, v74, v75
	v_cvt_pk_bf16_f32 v106, v64, v65
	v_cvt_pk_bf16_f32 v107, v68, v69
	v_cvt_pk_bf16_f32 v108, v60, v61
	v_cvt_pk_bf16_f32 v109, v66, v67
	v_cvt_pk_bf16_f32 v110, v56, v57
	v_cvt_pk_bf16_f32 v111, v58, v59
	v_cvt_pk_bf16_f32 v112, v112, v113
	v_cvt_pk_bf16_f32 v113, v118, v119
	v_cvt_pk_bf16_f32 v114, v114, v115
	v_cvt_pk_bf16_f32 v115, v116, v117
	v_cvt_pk_bf16_f32 v116, v78, v79
	v_cvt_pk_bf16_f32 v117, v76, v77
	v_cvt_pk_bf16_f32 v118, v72, v73
	v_cvt_pk_bf16_f32 v119, v62, v63
	v_cvt_pk_bf16_f32 v120, v52, v53
	v_cvt_pk_bf16_f32 v121, v54, v55
	v_cvt_pk_bf16_f32 v122, v46, v47
	v_cvt_pk_bf16_f32 v123, v50, v51
	v_cvt_pk_bf16_f32 v124, v44, v45
	v_cvt_pk_bf16_f32 v125, v48, v49
	v_cvt_pk_bf16_f32 v126, v40, v41
	v_cvt_pk_bf16_f32 v127, v42, v43
	v_readlane_b32 s100, v250, 8
	v_mbcnt_lo_u32_b32 v68, -1, 0
	v_mbcnt_hi_u32_b32 v68, -1, v68
	s_nop 1
	v_add_u32_e32 v69, s100, v68
	v_lshrrev_b32_e32 v70, 3, v69
	v_and_b32_e32 v71, 7, v69
	v_lshrrev_b32_e32 v72, 2, v71
	v_bfe_u32 v73, v71, 1, 1
	v_and_b32_e32 v74, 1, v71
	v_lshlrev_b32_e32 v74, 1, v74
	v_lshl_add_u32 v75, v72, 2, v74
	v_bfe_u32 v76, v70, 1, 3
	v_xor_b32_e32 v77, v75, v76
	v_add_u32_e32 v78, 1, v75
	v_xor_b32_e32 v78, v78, v76
	v_lshlrev_b32_e32 v79, 7, v70
	v_lshl_add_u32 v79, v73, 3, v79
	v_lshl_add_u32 v64, v77, 4, v79
	v_lshl_add_u32 v65, v78, 4, v79
	v_add_u32_e32 v66, 0x2000, v64
	v_add_u32_e32 v67, 0x2000, v65
	v_or_b32_e32 v81, v39, v80
	s_add_i32 s15, s10, 0x10000
	v_and_b32_e32 v82, 6, v137
	v_lshrrev_b32_e32 v84, 4, v136
	s_waitcnt vmcnt(0)
	s_waitcnt vmcnt(0)
	s_add_i32 s11, s10, 0x12000
	v_lshl_add_u32 v83, v139, 7, s10
	v_bitop3_b32 v85, v84, v82, 7 bitop3:0x6c
	v_and_b32_e32 v86, 8, v138
	v_or_b32_e32 v82, 1, v82
	v_add_u32_e32 v225, s15, v81
	s_waitcnt vmcnt(4)
	ds_write_b128 v225, v[24:27] offset:0
	v_lshlrev_b32_e32 v85, 4, v85
	v_add_u32_e32 v87, v83, v86
	v_bitop3_b32 v82, v84, v82, 7 bitop3:0x6c
	v_add3_u32 v226, v80, s11, v39
	ds_write_b128 v226, v[28:31] offset:0
	v_lshlrev_b32_e32 v82, 4, v82
	v_add_u32_e32 v227, v87, v85
	ds_write_b64 v64, v[12:13] offset:0
	v_lshrrev_b32_e32 v32, 5, v136
	v_add_u32_e32 v83, 0x2000, v83
	v_or_b32_e32 v84, v85, v86
	v_add_u32_e32 v228, v87, v82
	ds_write_b64 v65, v[14:15] offset:0
	v_xor_b32_e32 v32, v32, v137
	v_or_b32_e32 v86, v82, v86
	v_add_u32_e32 v229, v84, v83
	ds_write_b64 v66, v[4:5] offset:0
	v_lshlrev_b32_e32 v32, 4, v32
	v_add_u32_e32 v184, v86, v83
	ds_write_b64 v67, v[6:7] offset:0
	v_lshlrev_b32_e32 v33, 8, v143
	v_and_b32_e32 v32, 16, v32
	v_bfe_u32 v35, v137, 1, 3
	s_waitcnt vmcnt(4)
	ds_write_b128 v225, v[20:23] offset:0x4000
	v_lshlrev_b32_e32 v36, 5, v35
	v_add3_u32 v32, v33, s15, v32
	s_movk_i32 s16, 0x60
	ds_write_b128 v226, v[16:19] offset:0x4000
	v_xad_u32 v204, v36, s16, v32
	s_movk_i32 s16, 0x80
	ds_write_b64 v64, v[8:9] offset:0x4000
	v_xad_u32 v205, v36, s16, v32
	s_movk_i32 s16, 0xa0
	ds_write_b64 v65, v[10:11] offset:0x4000
	s_add_u32 s8, s6, 0x100
	v_xad_u32 v206, v36, s16, v32
	s_movk_i32 s16, 0xc0
	ds_write_b64 v66, v[0:1] offset:0x4000
	s_addc_u32 s9, s7, 0
	v_xad_u32 v207, v36, s16, v32
	s_movk_i32 s16, 0xe0
	ds_write_b64 v67, v[2:3] offset:0x4000
	v_add_u32_e32 v201, v32, v36
	v_xad_u32 v202, v36, 32, v32
	v_xad_u32 v203, v36, 64, v32
	v_xad_u32 v208, v36, s16, v32
	v_lshl_add_u32 v32, v143, 7, s10
	s_add_u32 s10, s78, 0x20000
	global_load_dwordx4 v[132:135], v198, s[8:9]
	s_addc_u32 s11, s79, 0
	global_load_dwordx4 v[128:131], v199, s[8:9]
	v_lshrrev_b32_e32 v34, 1, v137
	global_load_dwordx4 v[136:139], v196, s[10:11]
	s_add_u32 s6, s6, 0x180
	v_bitop3_b32 v34, v140, v34, 7 bitop3:0x78
	v_bitop3_b32 v37, v140, v35, 2 bitop3:0x36
	v_bitop3_b32 v38, v140, v35, 4 bitop3:0x36
	v_bitop3_b32 v35, v140, v35, 6 bitop3:0x36
	global_load_dwordx4 v[140:143], v197, s[10:11]
	s_addc_u32 s7, s7, 0
	s_add_u32 s8, s78, 0x30000
	global_load_dwordx4 v[148:151], v198, s[6:7]
	s_addc_u32 s9, s79, 0
	global_load_dwordx4 v[144:147], v199, s[6:7]
	global_load_dwordx4 v[152:155], v196, s[8:9]
	s_add_u32 s10, s13, s14
	global_load_dwordx4 v[156:159], v197, s[8:9]
	s_addc_u32 s11, s12, 0
	s_add_u32 s12, s41, s30
	v_mov_b32_e32 v0, 0
	s_mov_b32 s4, 0
	v_lshl_add_u32 v209, v34, 4, v32
	v_lshl_add_u32 v210, v37, 4, v32
	v_lshl_add_u32 v211, v38, 4, v32
	v_lshl_add_u32 v224, v35, 4, v32
	s_addc_u32 s13, 0, s31
	v_mov_b32_e32 v1, v0
	v_mov_b32_e32 v2, v0
	v_mov_b32_e32 v3, v0
	v_mov_b32_e32 v4, v0
	v_mov_b32_e32 v5, v0
	v_mov_b32_e32 v6, v0
	v_mov_b32_e32 v7, v0
	v_mov_b32_e32 v8, v0
	v_mov_b32_e32 v9, v0
	v_mov_b32_e32 v10, v0
	v_mov_b32_e32 v11, v0
	v_mov_b32_e32 v12, v0
	v_mov_b32_e32 v13, v0
	v_mov_b32_e32 v14, v0
	v_mov_b32_e32 v15, v0
	v_mov_b32_e32 v16, v0
	v_mov_b32_e32 v17, v0
	v_mov_b32_e32 v18, v0
	v_mov_b32_e32 v19, v0
	v_mov_b32_e32 v20, v0
	v_mov_b32_e32 v21, v0
	v_mov_b32_e32 v22, v0
	v_mov_b32_e32 v23, v0
	v_mov_b32_e32 v24, v0
	v_mov_b32_e32 v25, v0
	v_mov_b32_e32 v26, v0
	v_mov_b32_e32 v27, v0
	v_mov_b32_e32 v28, v0
	v_mov_b32_e32 v29, v0
	v_mov_b32_e32 v30, v0
	v_mov_b32_e32 v31, v0
	v_mov_b32_e32 v32, v0
	v_mov_b32_e32 v33, v0
	v_mov_b32_e32 v34, v0
	v_mov_b32_e32 v35, v0
	v_mov_b32_e32 v36, v0
	v_mov_b32_e32 v37, v0
	v_mov_b32_e32 v38, v0
	v_mov_b32_e32 v39, v0
	v_mov_b32_e32 v40, v0
	v_mov_b32_e32 v41, v0
	v_mov_b32_e32 v42, v0
	v_mov_b32_e32 v43, v0
	v_mov_b32_e32 v44, v0
	v_mov_b32_e32 v45, v0
	v_mov_b32_e32 v46, v0
	v_mov_b32_e32 v47, v0
	v_mov_b32_e32 v48, v0
	v_mov_b32_e32 v49, v0
	v_mov_b32_e32 v50, v0
	v_mov_b32_e32 v51, v0
	v_mov_b32_e32 v52, v0
	v_mov_b32_e32 v53, v0
	v_mov_b32_e32 v54, v0
	v_mov_b32_e32 v55, v0
	v_mov_b32_e32 v56, v0
	v_mov_b32_e32 v57, v0
	v_mov_b32_e32 v58, v0
	v_mov_b32_e32 v59, v0
	v_mov_b32_e32 v60, v0
	v_mov_b32_e32 v61, v0
	v_mov_b32_e32 v62, v0
	v_mov_b32_e32 v63, v0
	v_mov_b32_e32 v160, v0
	v_mov_b32_e32 v161, v0
	v_mov_b32_e32 v227, v64
	v_mov_b32_e32 v228, v65
	v_mov_b32_e32 v229, v66
	v_mov_b32_e32 v184, v67
	v_readlane_b32 s100, v250, 8
	v_mbcnt_lo_u32_b32 v68, -1, 0
	v_mbcnt_hi_u32_b32 v68, -1, v68
	v_and_b32_e32 v69, 15, v68
	v_lshrrev_b32_e32 v70, 4, v68
	v_lshlrev_b32_e32 v72, 8, v69
	v_add_u32_e32 v72, 0x10000, v72
	v_add_u32_e32 v71, 0, v70
	v_xor_b32_e32 v71, v71, v69
	v_lshl_add_u32 v201, v71, 4, v72
	v_add_u32_e32 v71, 4, v70
	v_xor_b32_e32 v71, v71, v69
	v_lshl_add_u32 v202, v71, 4, v72
	v_add_u32_e32 v71, 8, v70
	v_xor_b32_e32 v71, v71, v69
	v_lshl_add_u32 v203, v71, 4, v72
	v_add_u32_e32 v71, 12, v70
	v_xor_b32_e32 v71, v71, v69
	v_lshl_add_u32 v204, v71, 4, v72
	v_bfe_u32 v73, v69, 1, 3
	v_lshlrev_b32_e32 v76, 7, v69
	v_add_u32_e32 v71, 0, v70
	v_xor_b32_e32 v71, v71, v73
	v_lshl_add_u32 v209, v71, 4, v76
	v_add_u32_e32 v71, 4, v70
	v_xor_b32_e32 v71, v71, v73
	v_lshl_add_u32 v210, v71, 4, v76
	s_lshl_b32 s101, s100, 7
	s_add_u32 s101, s101, 0x8000
	s_cmpk_ge_u32 s100, 0x100
	s_cselect_b32 s6, 0x8000, 0
	s_add_u32 s101, s101, s6
	v_and_b32_e32 v74, 31, v68
	v_lshrrev_b32_e32 v75, 5, v68
	v_lshlrev_b32_e32 v74, 8, v74
	v_lshl_add_u32 v74, v75, 4, v74
	v_add_u32_e32 v74, s101, v74
	v_lshlrev_b32_e32 v75, 8, v69
	v_lshl_add_u32 v75, v70, 4, v75
	v_add_u32_e32 v75, s101, v75
	ds_write_b128 v74, v[96:99] offset:0
	ds_write_b128 v74, v[100:103] offset:32
	ds_write_b128 v74, v[104:107] offset:64
	ds_write_b128 v74, v[108:111] offset:96
	ds_write_b128 v74, v[112:115] offset:128
	ds_write_b128 v74, v[116:119] offset:160
	ds_write_b128 v74, v[120:123] offset:192
	ds_write_b128 v74, v[124:127] offset:224
	s_waitcnt lgkmcnt(0)
	ds_read_b128 v[96:99], v75 offset:0
	ds_read_b128 v[100:103], v75 offset:64
	ds_read_b128 v[104:107], v75 offset:128
	ds_read_b128 v[108:111], v75 offset:192
	ds_read_b128 v[112:115], v75 offset:4096
	ds_read_b128 v[116:119], v75 offset:4160
	ds_read_b128 v[120:123], v75 offset:4224
	ds_read_b128 v[124:127], v75 offset:4288
	s_waitcnt lgkmcnt(0)
	v_mov_b32_e32 v194, 0
	v_mov_b32_e32 v195, 0
	v_mov_b32_e32 v206, 0
	v_mov_b32_e32 v207, 0
.LBB0_734:
	s_waitcnt lgkmcnt(0)
	s_barrier
	ds_read_b128 v[160:163], v201 offset:0
	ds_read_b128 v[164:167], v202 offset:0
	ds_read_b128 v[168:171], v203 offset:0
	ds_read_b128 v[172:175], v204 offset:0
	ds_read_b128 v[176:179], v201 offset:4096
	ds_read_b128 v[180:183], v202 offset:4096
	ds_read_b128 v[230:233], v203 offset:4096
	s_waitcnt lgkmcnt(6)
	v_mfma_f32_16x16x32_bf16 v[64:67], v[160:163], v[96:99], 0
	v_mfma_f32_16x16x32_bf16 v[68:71], v[160:163], v[112:115], 0
	ds_read_b128 v[234:237], v204 offset:4096
	s_add_u32 s16, s22, s10
	s_addc_u32 s17, s23, s11
	s_add_u32 s15, s22, s12
	s_addc_u32 s14, s23, s13
	s_add_u32 s8, s16, 0x3bc00200
	s_addc_u32 s9, s17, 0
	s_add_u32 s6, s15, 0x23a40000
	s_addc_u32 s7, s14, 0
	s_waitcnt lgkmcnt(6)
	v_mfma_f32_16x16x32_bf16 v[68:71], v[164:167], v[116:119], v[68:71]
	v_mfma_f32_16x16x32_bf16 v[64:67], v[164:167], v[100:103], v[64:67]
	ds_read_b128 v[160:163], v201 offset:8192
	s_waitcnt vmcnt(4)
	ds_write_b128 v225, v[136:139] offset:32768
	s_waitcnt lgkmcnt(7)
	v_mfma_f32_16x16x32_bf16 v[64:67], v[168:171], v[104:107], v[64:67]
	v_mfma_f32_16x16x32_bf16 v[68:71], v[168:171], v[120:123], v[68:71]
	ds_read_b128 v[164:167], v202 offset:8192
	ds_write_b128 v226, v[140:143] offset:32768
	s_waitcnt lgkmcnt(8)
	v_mfma_f32_16x16x32_bf16 v[68:71], v[172:175], v[124:127], v[68:71]
	v_mfma_f32_16x16x32_bf16 v[64:67], v[172:175], v[108:111], v[64:67]
	ds_read_b128 v[168:171], v203 offset:8192
	ds_write_b64 v227, v[132:133] offset:32768
	s_waitcnt lgkmcnt(9)
	v_mfma_f32_16x16x32_bf16 v[72:75], v[176:179], v[96:99], 0
	v_mfma_f32_16x16x32_bf16 v[76:79], v[176:179], v[112:115], 0
	ds_read_b128 v[172:175], v204 offset:8192
	ds_write_b64 v228, v[134:135] offset:32768
	s_waitcnt lgkmcnt(10)
	v_mfma_f32_16x16x32_bf16 v[76:79], v[180:183], v[116:119], v[76:79]
	v_mfma_f32_16x16x32_bf16 v[72:75], v[180:183], v[100:103], v[72:75]
	ds_read_b128 v[176:179], v201 offset:12288
	ds_write_b64 v229, v[128:129] offset:32768
	s_waitcnt lgkmcnt(11)
	v_mfma_f32_16x16x32_bf16 v[72:75], v[230:233], v[104:107], v[72:75]
	v_mfma_f32_16x16x32_bf16 v[76:79], v[230:233], v[120:123], v[76:79]
	ds_read_b128 v[180:183], v202 offset:12288
	ds_write_b64 v184, v[130:131] offset:32768
	s_waitcnt lgkmcnt(12)
	v_mfma_f32_16x16x32_bf16 v[76:79], v[234:237], v[124:127], v[76:79]
	v_mfma_f32_16x16x32_bf16 v[72:75], v[234:237], v[108:111], v[72:75]
	ds_read_b128 v[230:233], v203 offset:12288
	global_load_dwordx4 v[132:135], v198, s[8:9]
	s_waitcnt lgkmcnt(12)
	v_mfma_f32_16x16x32_bf16 v[80:83], v[160:163], v[96:99], 0
	v_exp_f32_e32 v64, v64
	v_exp_f32_e32 v65, v65
	v_exp_f32_e32 v66, v66
	v_mfma_f32_16x16x32_bf16 v[84:87], v[160:163], v[112:115], 0
	v_exp_f32_e32 v67, v67
	v_exp_f32_e32 v68, v68
	v_exp_f32_e32 v69, v69
	ds_read_b128 v[234:237], v204 offset:12288
	global_load_dwordx4 v[128:131], v199, s[8:9]
	s_waitcnt lgkmcnt(11)
	v_mfma_f32_16x16x32_bf16 v[84:87], v[164:167], v[116:119], v[84:87]
	v_exp_f32_e32 v70, v70
	v_exp_f32_e32 v71, v71
	v_add_f32_e32 v194, v194, v64
	v_mfma_f32_16x16x32_bf16 v[80:83], v[164:167], v[100:103], v[80:83]
	v_add_f32_e32 v194, v194, v65
	v_add_f32_e32 v194, v194, v66
	v_add_f32_e32 v194, v194, v67
	ds_read_b128 v[160:163], v209 offset:0
	global_load_dwordx4 v[136:139], v196, s[6:7]
	s_waitcnt lgkmcnt(10)
	v_mfma_f32_16x16x32_bf16 v[80:83], v[168:171], v[104:107], v[80:83]
	v_add_f32_e32 v195, v195, v68
	v_add_f32_e32 v195, v195, v69
	v_add_f32_e32 v195, v195, v70
	v_mfma_f32_16x16x32_bf16 v[84:87], v[168:171], v[120:123], v[84:87]
	v_add_f32_e32 v195, v195, v71
	v_cvt_pk_bf16_f32 v64, v64, v65
	v_cvt_pk_bf16_f32 v65, v66, v67
	ds_read_b128 v[164:167], v209 offset:2048
	global_load_dwordx4 v[140:143], v197, s[6:7]
	s_waitcnt lgkmcnt(9)
	v_mfma_f32_16x16x32_bf16 v[84:87], v[172:175], v[124:127], v[84:87]
	v_cvt_pk_bf16_f32 v68, v68, v69
	v_cvt_pk_bf16_f32 v69, v70, v71
	v_mfma_f32_16x16x32_bf16 v[80:83], v[172:175], v[108:111], v[80:83]
	ds_read_b128 v[168:171], v209 offset:4096
	s_waitcnt lgkmcnt(8)
	v_mfma_f32_16x16x32_bf16 v[88:91], v[176:179], v[96:99], 0
	v_exp_f32_e32 v72, v72
	v_exp_f32_e32 v73, v73
	v_exp_f32_e32 v74, v74
	v_mfma_f32_16x16x32_bf16 v[92:95], v[176:179], v[112:115], 0
	v_exp_f32_e32 v75, v75
	v_exp_f32_e32 v76, v76
	v_exp_f32_e32 v77, v77
	ds_read_b128 v[172:175], v209 offset:6144
	s_waitcnt lgkmcnt(7)
	v_mfma_f32_16x16x32_bf16 v[92:95], v[180:183], v[116:119], v[92:95]
	v_exp_f32_e32 v78, v78
	v_exp_f32_e32 v79, v79
	v_add_f32_e32 v194, v194, v72
	v_mfma_f32_16x16x32_bf16 v[88:91], v[180:183], v[100:103], v[88:91]
	v_add_f32_e32 v194, v194, v73
	v_add_f32_e32 v194, v194, v74
	v_add_f32_e32 v194, v194, v75
	ds_read_b128 v[176:179], v209 offset:8192
	s_waitcnt lgkmcnt(6)
	v_mfma_f32_16x16x32_bf16 v[88:91], v[230:233], v[104:107], v[88:91]
	v_add_f32_e32 v195, v195, v76
	v_add_f32_e32 v195, v195, v77
	v_add_f32_e32 v195, v195, v78
	v_mfma_f32_16x16x32_bf16 v[92:95], v[230:233], v[120:123], v[92:95]
	v_add_f32_e32 v195, v195, v79
	v_cvt_pk_bf16_f32 v66, v72, v73
	v_cvt_pk_bf16_f32 v67, v74, v75
	ds_read_b128 v[180:183], v209 offset:10240
	s_waitcnt lgkmcnt(6)
	v_mfma_f32_16x16x32_bf16 v[92:95], v[234:237], v[124:127], v[92:95]
	v_cvt_pk_bf16_f32 v70, v76, v77
	v_cvt_pk_bf16_f32 v71, v78, v79
	v_mfma_f32_16x16x32_bf16 v[88:91], v[234:237], v[108:111], v[88:91]
	ds_read_b128 v[230:233], v209 offset:12288
	s_waitcnt lgkmcnt(6)
	v_mfma_f32_16x16x32_bf16 v[0:3], v[160:163], v[64:67], v[0:3]
	v_exp_f32_e32 v80, v80
	v_exp_f32_e32 v81, v81
	v_exp_f32_e32 v82, v82
	v_mfma_f32_16x16x32_bf16 v[4:7], v[160:163], v[68:71], v[4:7]
	v_exp_f32_e32 v83, v83
	v_exp_f32_e32 v84, v84
	v_exp_f32_e32 v85, v85
	ds_read_b128 v[234:237], v209 offset:14336
	s_waitcnt lgkmcnt(6)
	v_mfma_f32_16x16x32_bf16 v[12:15], v[164:167], v[68:71], v[12:15]
	v_exp_f32_e32 v86, v86
	v_exp_f32_e32 v87, v87
	v_add_f32_e32 v194, v194, v80
	v_mfma_f32_16x16x32_bf16 v[8:11], v[164:167], v[64:67], v[8:11]
	v_add_f32_e32 v194, v194, v81
	v_add_f32_e32 v194, v194, v82
	v_add_f32_e32 v194, v194, v83
	ds_read_b128 v[160:163], v210 offset:0
	s_waitcnt lgkmcnt(6)
	v_mfma_f32_16x16x32_bf16 v[16:19], v[168:171], v[64:67], v[16:19]
	v_add_f32_e32 v195, v195, v84
	v_add_f32_e32 v195, v195, v85
	v_add_f32_e32 v195, v195, v86
	v_mfma_f32_16x16x32_bf16 v[20:23], v[168:171], v[68:71], v[20:23]
	v_add_f32_e32 v195, v195, v87
	v_cvt_pk_bf16_f32 v80, v80, v81
	v_cvt_pk_bf16_f32 v81, v82, v83
	ds_read_b128 v[164:167], v210 offset:2048
	s_waitcnt lgkmcnt(6)
	v_mfma_f32_16x16x32_bf16 v[28:31], v[172:175], v[68:71], v[28:31]
	v_cvt_pk_bf16_f32 v84, v84, v85
	v_cvt_pk_bf16_f32 v85, v86, v87
	v_mfma_f32_16x16x32_bf16 v[24:27], v[172:175], v[64:67], v[24:27]
	ds_read_b128 v[168:171], v210 offset:4096
	s_waitcnt lgkmcnt(6)
	v_mfma_f32_16x16x32_bf16 v[32:35], v[176:179], v[64:67], v[32:35]
	v_exp_f32_e32 v88, v88
	v_exp_f32_e32 v89, v89
	v_exp_f32_e32 v90, v90
	v_mfma_f32_16x16x32_bf16 v[36:39], v[176:179], v[68:71], v[36:39]
	v_exp_f32_e32 v91, v91
	v_exp_f32_e32 v92, v92
	v_exp_f32_e32 v93, v93
	ds_read_b128 v[172:175], v210 offset:6144
	s_waitcnt lgkmcnt(6)
	v_mfma_f32_16x16x32_bf16 v[44:47], v[180:183], v[68:71], v[44:47]
	v_exp_f32_e32 v94, v94
	v_exp_f32_e32 v95, v95
	v_add_f32_e32 v194, v194, v88
	v_mfma_f32_16x16x32_bf16 v[40:43], v[180:183], v[64:67], v[40:43]
	v_add_f32_e32 v194, v194, v89
	v_add_f32_e32 v194, v194, v90
	v_add_f32_e32 v194, v194, v91
	ds_read_b128 v[176:179], v210 offset:8192
	s_waitcnt lgkmcnt(6)
	v_mfma_f32_16x16x32_bf16 v[48:51], v[230:233], v[64:67], v[48:51]
	v_add_f32_e32 v195, v195, v92
	v_add_f32_e32 v195, v195, v93
	v_add_f32_e32 v195, v195, v94
	v_mfma_f32_16x16x32_bf16 v[52:55], v[230:233], v[68:71], v[52:55]
	v_add_f32_e32 v195, v195, v95
	v_cvt_pk_bf16_f32 v82, v88, v89
	v_cvt_pk_bf16_f32 v83, v90, v91
	ds_read_b128 v[180:183], v210 offset:10240
	s_waitcnt lgkmcnt(6)
	v_mfma_f32_16x16x32_bf16 v[60:63], v[234:237], v[68:71], v[60:63]
	v_cvt_pk_bf16_f32 v86, v92, v93
	v_cvt_pk_bf16_f32 v87, v94, v95
	v_mfma_f32_16x16x32_bf16 v[56:59], v[234:237], v[64:67], v[56:59]
	ds_read_b128 v[230:233], v210 offset:12288
	s_waitcnt lgkmcnt(6)
	v_mfma_f32_16x16x32_bf16 v[0:3], v[160:163], v[80:83], v[0:3]
	v_mfma_f32_16x16x32_bf16 v[4:7], v[160:163], v[84:87], v[4:7]
	ds_read_b128 v[234:237], v210 offset:14336
	s_waitcnt lgkmcnt(6)
	v_mfma_f32_16x16x32_bf16 v[12:15], v[164:167], v[84:87], v[12:15]
	v_mfma_f32_16x16x32_bf16 v[8:11], v[164:167], v[80:83], v[8:11]
	ds_read_b128 v[160:163], v201 offset:16384
	s_waitcnt lgkmcnt(6)
	v_mfma_f32_16x16x32_bf16 v[16:19], v[168:171], v[80:83], v[16:19]
	v_mfma_f32_16x16x32_bf16 v[20:23], v[168:171], v[84:87], v[20:23]
	ds_read_b128 v[164:167], v202 offset:16384
	s_waitcnt lgkmcnt(6)
	v_mfma_f32_16x16x32_bf16 v[28:31], v[172:175], v[84:87], v[28:31]
	v_mfma_f32_16x16x32_bf16 v[24:27], v[172:175], v[80:83], v[24:27]
	ds_read_b128 v[168:171], v203 offset:16384
	s_waitcnt lgkmcnt(6)
	v_mfma_f32_16x16x32_bf16 v[32:35], v[176:179], v[80:83], v[32:35]
	v_mfma_f32_16x16x32_bf16 v[36:39], v[176:179], v[84:87], v[36:39]
	ds_read_b128 v[172:175], v204 offset:16384
	s_waitcnt lgkmcnt(6)
	v_mfma_f32_16x16x32_bf16 v[44:47], v[180:183], v[84:87], v[44:47]
	v_mfma_f32_16x16x32_bf16 v[40:43], v[180:183], v[80:83], v[40:43]
	ds_read_b128 v[176:179], v201 offset:20480
	s_waitcnt lgkmcnt(6)
	v_mfma_f32_16x16x32_bf16 v[48:51], v[230:233], v[80:83], v[48:51]
	v_mfma_f32_16x16x32_bf16 v[52:55], v[230:233], v[84:87], v[52:55]
	ds_read_b128 v[180:183], v202 offset:20480
	s_waitcnt lgkmcnt(6)
	v_mfma_f32_16x16x32_bf16 v[60:63], v[234:237], v[84:87], v[60:63]
	v_mfma_f32_16x16x32_bf16 v[56:59], v[234:237], v[80:83], v[56:59]
	ds_read_b128 v[230:233], v203 offset:20480
	s_waitcnt lgkmcnt(6)
	v_mfma_f32_16x16x32_bf16 v[64:67], v[160:163], v[96:99], 0
	v_mfma_f32_16x16x32_bf16 v[68:71], v[160:163], v[112:115], 0
	ds_read_b128 v[234:237], v204 offset:20480
	s_add_u32 s8, s16, 0x3bc00280
	s_addc_u32 s9, s17, 0
	s_add_u32 s6, s15, 0x23a50000
	s_addc_u32 s7, s14, 0
	s_waitcnt lgkmcnt(6)
	v_mfma_f32_16x16x32_bf16 v[68:71], v[164:167], v[116:119], v[68:71]
	v_mfma_f32_16x16x32_bf16 v[64:67], v[164:167], v[100:103], v[64:67]
	ds_read_b128 v[160:163], v201 offset:24576
	s_waitcnt vmcnt(4)
	ds_write_b128 v225, v[152:155] offset:49152
	s_waitcnt lgkmcnt(7)
	v_mfma_f32_16x16x32_bf16 v[64:67], v[168:171], v[104:107], v[64:67]
	v_mfma_f32_16x16x32_bf16 v[68:71], v[168:171], v[120:123], v[68:71]
	ds_read_b128 v[164:167], v202 offset:24576
	ds_write_b128 v226, v[156:159] offset:49152
	s_waitcnt lgkmcnt(8)
	v_mfma_f32_16x16x32_bf16 v[68:71], v[172:175], v[124:127], v[68:71]
	v_mfma_f32_16x16x32_bf16 v[64:67], v[172:175], v[108:111], v[64:67]
	ds_read_b128 v[168:171], v203 offset:24576
	ds_write_b64 v227, v[148:149] offset:49152
	s_waitcnt lgkmcnt(9)
	v_mfma_f32_16x16x32_bf16 v[72:75], v[176:179], v[96:99], 0
	v_mfma_f32_16x16x32_bf16 v[76:79], v[176:179], v[112:115], 0
	ds_read_b128 v[172:175], v204 offset:24576
	ds_write_b64 v228, v[150:151] offset:49152
	s_waitcnt lgkmcnt(10)
	v_mfma_f32_16x16x32_bf16 v[76:79], v[180:183], v[116:119], v[76:79]
	v_mfma_f32_16x16x32_bf16 v[72:75], v[180:183], v[100:103], v[72:75]
	ds_read_b128 v[176:179], v201 offset:28672
	ds_write_b64 v229, v[144:145] offset:49152
	s_waitcnt lgkmcnt(11)
	v_mfma_f32_16x16x32_bf16 v[72:75], v[230:233], v[104:107], v[72:75]
	v_mfma_f32_16x16x32_bf16 v[76:79], v[230:233], v[120:123], v[76:79]
	ds_read_b128 v[180:183], v202 offset:28672
	ds_write_b64 v184, v[146:147] offset:49152
	s_waitcnt lgkmcnt(12)
	v_mfma_f32_16x16x32_bf16 v[76:79], v[234:237], v[124:127], v[76:79]
	v_mfma_f32_16x16x32_bf16 v[72:75], v[234:237], v[108:111], v[72:75]
	ds_read_b128 v[230:233], v203 offset:28672
	global_load_dwordx4 v[148:151], v198, s[8:9]
	s_waitcnt lgkmcnt(12)
	v_mfma_f32_16x16x32_bf16 v[80:83], v[160:163], v[96:99], 0
	v_exp_f32_e32 v64, v64
	v_exp_f32_e32 v65, v65
	v_exp_f32_e32 v66, v66
	v_mfma_f32_16x16x32_bf16 v[84:87], v[160:163], v[112:115], 0
	v_exp_f32_e32 v67, v67
	v_exp_f32_e32 v68, v68
	v_exp_f32_e32 v69, v69
	ds_read_b128 v[234:237], v204 offset:28672
	global_load_dwordx4 v[144:147], v199, s[8:9]
	s_waitcnt lgkmcnt(11)
	v_mfma_f32_16x16x32_bf16 v[84:87], v[164:167], v[116:119], v[84:87]
	v_exp_f32_e32 v70, v70
	v_exp_f32_e32 v71, v71
	v_add_f32_e32 v194, v194, v64
	v_mfma_f32_16x16x32_bf16 v[80:83], v[164:167], v[100:103], v[80:83]
	v_add_f32_e32 v194, v194, v65
	v_add_f32_e32 v194, v194, v66
	v_add_f32_e32 v194, v194, v67
	ds_read_b128 v[160:163], v209 offset:16384
	global_load_dwordx4 v[152:155], v196, s[6:7]
	s_waitcnt lgkmcnt(10)
	v_mfma_f32_16x16x32_bf16 v[80:83], v[168:171], v[104:107], v[80:83]
	v_add_f32_e32 v195, v195, v68
	v_add_f32_e32 v195, v195, v69
	v_add_f32_e32 v195, v195, v70
	v_mfma_f32_16x16x32_bf16 v[84:87], v[168:171], v[120:123], v[84:87]
	v_add_f32_e32 v195, v195, v71
	v_cvt_pk_bf16_f32 v64, v64, v65
	v_cvt_pk_bf16_f32 v65, v66, v67
	ds_read_b128 v[164:167], v209 offset:18432
	global_load_dwordx4 v[156:159], v197, s[6:7]
	s_waitcnt lgkmcnt(9)
	v_mfma_f32_16x16x32_bf16 v[84:87], v[172:175], v[124:127], v[84:87]
	v_cvt_pk_bf16_f32 v68, v68, v69
	v_cvt_pk_bf16_f32 v69, v70, v71
	v_mfma_f32_16x16x32_bf16 v[80:83], v[172:175], v[108:111], v[80:83]
	ds_read_b128 v[168:171], v209 offset:20480
	s_waitcnt lgkmcnt(8)
	v_mfma_f32_16x16x32_bf16 v[88:91], v[176:179], v[96:99], 0
	v_exp_f32_e32 v72, v72
	v_exp_f32_e32 v73, v73
	v_exp_f32_e32 v74, v74
	v_mfma_f32_16x16x32_bf16 v[92:95], v[176:179], v[112:115], 0
	v_exp_f32_e32 v75, v75
	v_exp_f32_e32 v76, v76
	v_exp_f32_e32 v77, v77
	ds_read_b128 v[172:175], v209 offset:22528
	s_waitcnt lgkmcnt(7)
	v_mfma_f32_16x16x32_bf16 v[92:95], v[180:183], v[116:119], v[92:95]
	v_exp_f32_e32 v78, v78
	v_exp_f32_e32 v79, v79
	v_add_f32_e32 v194, v194, v72
	v_mfma_f32_16x16x32_bf16 v[88:91], v[180:183], v[100:103], v[88:91]
	v_add_f32_e32 v194, v194, v73
	v_add_f32_e32 v194, v194, v74
	v_add_f32_e32 v194, v194, v75
	ds_read_b128 v[176:179], v209 offset:24576
	s_waitcnt lgkmcnt(6)
	v_mfma_f32_16x16x32_bf16 v[88:91], v[230:233], v[104:107], v[88:91]
	v_add_f32_e32 v195, v195, v76
	v_add_f32_e32 v195, v195, v77
	v_add_f32_e32 v195, v195, v78
	v_mfma_f32_16x16x32_bf16 v[92:95], v[230:233], v[120:123], v[92:95]
	v_add_f32_e32 v195, v195, v79
	v_cvt_pk_bf16_f32 v66, v72, v73
	v_cvt_pk_bf16_f32 v67, v74, v75
	ds_read_b128 v[180:183], v209 offset:26624
	s_waitcnt lgkmcnt(6)
	v_mfma_f32_16x16x32_bf16 v[92:95], v[234:237], v[124:127], v[92:95]
	v_cvt_pk_bf16_f32 v70, v76, v77
	v_cvt_pk_bf16_f32 v71, v78, v79
	v_mfma_f32_16x16x32_bf16 v[88:91], v[234:237], v[108:111], v[88:91]
	ds_read_b128 v[230:233], v209 offset:28672
	s_waitcnt lgkmcnt(6)
	v_mfma_f32_16x16x32_bf16 v[0:3], v[160:163], v[64:67], v[0:3]
	v_exp_f32_e32 v80, v80
	v_exp_f32_e32 v81, v81
	v_exp_f32_e32 v82, v82
	v_mfma_f32_16x16x32_bf16 v[4:7], v[160:163], v[68:71], v[4:7]
	v_exp_f32_e32 v83, v83
	v_exp_f32_e32 v84, v84
	v_exp_f32_e32 v85, v85
	ds_read_b128 v[234:237], v209 offset:30720
	s_waitcnt lgkmcnt(6)
	v_mfma_f32_16x16x32_bf16 v[12:15], v[164:167], v[68:71], v[12:15]
	v_exp_f32_e32 v86, v86
	v_exp_f32_e32 v87, v87
	v_add_f32_e32 v194, v194, v80
	v_mfma_f32_16x16x32_bf16 v[8:11], v[164:167], v[64:67], v[8:11]
	v_add_f32_e32 v194, v194, v81
	v_add_f32_e32 v194, v194, v82
	v_add_f32_e32 v194, v194, v83
	ds_read_b128 v[160:163], v210 offset:16384
	s_waitcnt lgkmcnt(6)
	v_mfma_f32_16x16x32_bf16 v[16:19], v[168:171], v[64:67], v[16:19]
	v_add_f32_e32 v195, v195, v84
	v_add_f32_e32 v195, v195, v85
	v_add_f32_e32 v195, v195, v86
	v_mfma_f32_16x16x32_bf16 v[20:23], v[168:171], v[68:71], v[20:23]
	v_add_f32_e32 v195, v195, v87
	v_cvt_pk_bf16_f32 v80, v80, v81
	v_cvt_pk_bf16_f32 v81, v82, v83
	ds_read_b128 v[164:167], v210 offset:18432
	s_waitcnt lgkmcnt(6)
	v_mfma_f32_16x16x32_bf16 v[28:31], v[172:175], v[68:71], v[28:31]
	v_cvt_pk_bf16_f32 v84, v84, v85
	v_cvt_pk_bf16_f32 v85, v86, v87
	v_mfma_f32_16x16x32_bf16 v[24:27], v[172:175], v[64:67], v[24:27]
	ds_read_b128 v[168:171], v210 offset:20480
	s_waitcnt lgkmcnt(6)
	v_mfma_f32_16x16x32_bf16 v[32:35], v[176:179], v[64:67], v[32:35]
	v_exp_f32_e32 v88, v88
	v_exp_f32_e32 v89, v89
	v_exp_f32_e32 v90, v90
	v_mfma_f32_16x16x32_bf16 v[36:39], v[176:179], v[68:71], v[36:39]
	v_exp_f32_e32 v91, v91
	v_exp_f32_e32 v92, v92
	v_exp_f32_e32 v93, v93
	ds_read_b128 v[172:175], v210 offset:22528
	s_waitcnt lgkmcnt(6)
	v_mfma_f32_16x16x32_bf16 v[44:47], v[180:183], v[68:71], v[44:47]
	v_exp_f32_e32 v94, v94
	v_exp_f32_e32 v95, v95
	v_add_f32_e32 v194, v194, v88
	v_mfma_f32_16x16x32_bf16 v[40:43], v[180:183], v[64:67], v[40:43]
	v_add_f32_e32 v194, v194, v89
	v_add_f32_e32 v194, v194, v90
	v_add_f32_e32 v194, v194, v91
	ds_read_b128 v[176:179], v210 offset:24576
	s_waitcnt lgkmcnt(6)
	v_mfma_f32_16x16x32_bf16 v[48:51], v[230:233], v[64:67], v[48:51]
	v_add_f32_e32 v195, v195, v92
	v_add_f32_e32 v195, v195, v93
	v_add_f32_e32 v195, v195, v94
	v_mfma_f32_16x16x32_bf16 v[52:55], v[230:233], v[68:71], v[52:55]
	v_add_f32_e32 v195, v195, v95
	v_cvt_pk_bf16_f32 v82, v88, v89
	v_cvt_pk_bf16_f32 v83, v90, v91
	ds_read_b128 v[180:183], v210 offset:26624
	s_waitcnt lgkmcnt(6)
	v_mfma_f32_16x16x32_bf16 v[60:63], v[234:237], v[68:71], v[60:63]
	v_cvt_pk_bf16_f32 v86, v92, v93
	v_cvt_pk_bf16_f32 v87, v94, v95
	v_mfma_f32_16x16x32_bf16 v[56:59], v[234:237], v[64:67], v[56:59]
	ds_read_b128 v[230:233], v210 offset:28672
	s_waitcnt lgkmcnt(6)
	v_mfma_f32_16x16x32_bf16 v[0:3], v[160:163], v[80:83], v[0:3]
	v_mfma_f32_16x16x32_bf16 v[4:7], v[160:163], v[84:87], v[4:7]
	ds_read_b128 v[234:237], v210 offset:30720
	s_waitcnt lgkmcnt(6)
	v_mfma_f32_16x16x32_bf16 v[12:15], v[164:167], v[84:87], v[12:15]
	v_mfma_f32_16x16x32_bf16 v[8:11], v[164:167], v[80:83], v[8:11]
	s_waitcnt lgkmcnt(5)
	v_mfma_f32_16x16x32_bf16 v[16:19], v[168:171], v[80:83], v[16:19]
	v_mfma_f32_16x16x32_bf16 v[20:23], v[168:171], v[84:87], v[20:23]
	s_waitcnt lgkmcnt(4)
	v_mfma_f32_16x16x32_bf16 v[28:31], v[172:175], v[84:87], v[28:31]
	v_mfma_f32_16x16x32_bf16 v[24:27], v[172:175], v[80:83], v[24:27]
	s_waitcnt lgkmcnt(3)
	v_mfma_f32_16x16x32_bf16 v[32:35], v[176:179], v[80:83], v[32:35]
	v_mfma_f32_16x16x32_bf16 v[36:39], v[176:179], v[84:87], v[36:39]
	s_waitcnt lgkmcnt(2)
	v_mfma_f32_16x16x32_bf16 v[44:47], v[180:183], v[84:87], v[44:47]
	v_mfma_f32_16x16x32_bf16 v[40:43], v[180:183], v[80:83], v[40:43]
	s_waitcnt lgkmcnt(1)
	v_mfma_f32_16x16x32_bf16 v[48:51], v[230:233], v[80:83], v[48:51]
	v_mfma_f32_16x16x32_bf16 v[52:55], v[230:233], v[84:87], v[52:55]
	s_waitcnt lgkmcnt(0)
	v_mfma_f32_16x16x32_bf16 v[60:63], v[234:237], v[84:87], v[60:63]
	v_mfma_f32_16x16x32_bf16 v[56:59], v[234:237], v[80:83], v[56:59]
	s_waitcnt lgkmcnt(0)
	s_barrier
	ds_read_b128 v[160:163], v201 offset:32768
	ds_read_b128 v[164:167], v202 offset:32768
	ds_read_b128 v[168:171], v203 offset:32768
	ds_read_b128 v[172:175], v204 offset:32768
	ds_read_b128 v[176:179], v201 offset:36864
	ds_read_b128 v[180:183], v202 offset:36864
	ds_read_b128 v[230:233], v203 offset:36864
	s_waitcnt lgkmcnt(6)
	v_mfma_f32_16x16x32_bf16 v[64:67], v[160:163], v[96:99], 0
	v_mfma_f32_16x16x32_bf16 v[68:71], v[160:163], v[112:115], 0
	ds_read_b128 v[234:237], v204 offset:36864
	s_add_u32 s8, s16, 0x3bc00300
	s_addc_u32 s9, s17, 0
	s_add_u32 s6, s15, 0x23a60000
	s_addc_u32 s7, s14, 0
	s_waitcnt lgkmcnt(6)
	v_mfma_f32_16x16x32_bf16 v[68:71], v[164:167], v[116:119], v[68:71]
	v_mfma_f32_16x16x32_bf16 v[64:67], v[164:167], v[100:103], v[64:67]
	ds_read_b128 v[160:163], v201 offset:40960
	s_waitcnt vmcnt(4)
	ds_write_b128 v225, v[136:139] offset:0
	s_waitcnt lgkmcnt(7)
	v_mfma_f32_16x16x32_bf16 v[64:67], v[168:171], v[104:107], v[64:67]
	v_mfma_f32_16x16x32_bf16 v[68:71], v[168:171], v[120:123], v[68:71]
	ds_read_b128 v[164:167], v202 offset:40960
	ds_write_b128 v226, v[140:143] offset:0
	s_waitcnt lgkmcnt(8)
	v_mfma_f32_16x16x32_bf16 v[68:71], v[172:175], v[124:127], v[68:71]
	v_mfma_f32_16x16x32_bf16 v[64:67], v[172:175], v[108:111], v[64:67]
	ds_read_b128 v[168:171], v203 offset:40960
	ds_write_b64 v227, v[132:133] offset:0
	s_waitcnt lgkmcnt(9)
	v_mfma_f32_16x16x32_bf16 v[72:75], v[176:179], v[96:99], 0
	v_mfma_f32_16x16x32_bf16 v[76:79], v[176:179], v[112:115], 0
	ds_read_b128 v[172:175], v204 offset:40960
	ds_write_b64 v228, v[134:135] offset:0
	s_waitcnt lgkmcnt(10)
	v_mfma_f32_16x16x32_bf16 v[76:79], v[180:183], v[116:119], v[76:79]
	v_mfma_f32_16x16x32_bf16 v[72:75], v[180:183], v[100:103], v[72:75]
	ds_read_b128 v[176:179], v201 offset:45056
	ds_write_b64 v229, v[128:129] offset:0
	s_waitcnt lgkmcnt(11)
	v_mfma_f32_16x16x32_bf16 v[72:75], v[230:233], v[104:107], v[72:75]
	v_mfma_f32_16x16x32_bf16 v[76:79], v[230:233], v[120:123], v[76:79]
	ds_read_b128 v[180:183], v202 offset:45056
	ds_write_b64 v184, v[130:131] offset:0
	s_waitcnt lgkmcnt(12)
	v_mfma_f32_16x16x32_bf16 v[76:79], v[234:237], v[124:127], v[76:79]
	v_mfma_f32_16x16x32_bf16 v[72:75], v[234:237], v[108:111], v[72:75]
	ds_read_b128 v[230:233], v203 offset:45056
	global_load_dwordx4 v[132:135], v198, s[8:9]
	s_waitcnt lgkmcnt(12)
	v_mfma_f32_16x16x32_bf16 v[80:83], v[160:163], v[96:99], 0
	v_exp_f32_e32 v64, v64
	v_exp_f32_e32 v65, v65
	v_exp_f32_e32 v66, v66
	v_mfma_f32_16x16x32_bf16 v[84:87], v[160:163], v[112:115], 0
	v_exp_f32_e32 v67, v67
	v_exp_f32_e32 v68, v68
	v_exp_f32_e32 v69, v69
	ds_read_b128 v[234:237], v204 offset:45056
	global_load_dwordx4 v[128:131], v199, s[8:9]
	s_waitcnt lgkmcnt(11)
	v_mfma_f32_16x16x32_bf16 v[84:87], v[164:167], v[116:119], v[84:87]
	v_exp_f32_e32 v70, v70
	v_exp_f32_e32 v71, v71
	v_add_f32_e32 v194, v194, v64
	v_mfma_f32_16x16x32_bf16 v[80:83], v[164:167], v[100:103], v[80:83]
	v_add_f32_e32 v194, v194, v65
	v_add_f32_e32 v194, v194, v66
	v_add_f32_e32 v194, v194, v67
	ds_read_b128 v[160:163], v209 offset:32768
	global_load_dwordx4 v[136:139], v196, s[6:7]
	s_waitcnt lgkmcnt(10)
	v_mfma_f32_16x16x32_bf16 v[80:83], v[168:171], v[104:107], v[80:83]
	v_add_f32_e32 v195, v195, v68
	v_add_f32_e32 v195, v195, v69
	v_add_f32_e32 v195, v195, v70
	v_mfma_f32_16x16x32_bf16 v[84:87], v[168:171], v[120:123], v[84:87]
	v_add_f32_e32 v195, v195, v71
	v_cvt_pk_bf16_f32 v64, v64, v65
	v_cvt_pk_bf16_f32 v65, v66, v67
	ds_read_b128 v[164:167], v209 offset:34816
	global_load_dwordx4 v[140:143], v197, s[6:7]
	s_waitcnt lgkmcnt(9)
	v_mfma_f32_16x16x32_bf16 v[84:87], v[172:175], v[124:127], v[84:87]
	v_cvt_pk_bf16_f32 v68, v68, v69
	v_cvt_pk_bf16_f32 v69, v70, v71
	v_mfma_f32_16x16x32_bf16 v[80:83], v[172:175], v[108:111], v[80:83]
	ds_read_b128 v[168:171], v209 offset:36864
	s_waitcnt lgkmcnt(8)
	v_mfma_f32_16x16x32_bf16 v[88:91], v[176:179], v[96:99], 0
	v_exp_f32_e32 v72, v72
	v_exp_f32_e32 v73, v73
	v_exp_f32_e32 v74, v74
	v_mfma_f32_16x16x32_bf16 v[92:95], v[176:179], v[112:115], 0
	v_exp_f32_e32 v75, v75
	v_exp_f32_e32 v76, v76
	v_exp_f32_e32 v77, v77
	ds_read_b128 v[172:175], v209 offset:38912
	s_waitcnt lgkmcnt(7)
	v_mfma_f32_16x16x32_bf16 v[92:95], v[180:183], v[116:119], v[92:95]
	v_exp_f32_e32 v78, v78
	v_exp_f32_e32 v79, v79
	v_add_f32_e32 v194, v194, v72
	v_mfma_f32_16x16x32_bf16 v[88:91], v[180:183], v[100:103], v[88:91]
	v_add_f32_e32 v194, v194, v73
	v_add_f32_e32 v194, v194, v74
	v_add_f32_e32 v194, v194, v75
	ds_read_b128 v[176:179], v209 offset:40960
	s_waitcnt lgkmcnt(6)
	v_mfma_f32_16x16x32_bf16 v[88:91], v[230:233], v[104:107], v[88:91]
	v_add_f32_e32 v195, v195, v76
	v_add_f32_e32 v195, v195, v77
	v_add_f32_e32 v195, v195, v78
	v_mfma_f32_16x16x32_bf16 v[92:95], v[230:233], v[120:123], v[92:95]
	v_add_f32_e32 v195, v195, v79
	v_cvt_pk_bf16_f32 v66, v72, v73
	v_cvt_pk_bf16_f32 v67, v74, v75
	ds_read_b128 v[180:183], v209 offset:43008
	s_waitcnt lgkmcnt(6)
	v_mfma_f32_16x16x32_bf16 v[92:95], v[234:237], v[124:127], v[92:95]
	v_cvt_pk_bf16_f32 v70, v76, v77
	v_cvt_pk_bf16_f32 v71, v78, v79
	v_mfma_f32_16x16x32_bf16 v[88:91], v[234:237], v[108:111], v[88:91]
	ds_read_b128 v[230:233], v209 offset:45056
	s_waitcnt lgkmcnt(6)
	v_mfma_f32_16x16x32_bf16 v[0:3], v[160:163], v[64:67], v[0:3]
	v_exp_f32_e32 v80, v80
	v_exp_f32_e32 v81, v81
	v_exp_f32_e32 v82, v82
	v_mfma_f32_16x16x32_bf16 v[4:7], v[160:163], v[68:71], v[4:7]
	v_exp_f32_e32 v83, v83
	v_exp_f32_e32 v84, v84
	v_exp_f32_e32 v85, v85
	ds_read_b128 v[234:237], v209 offset:47104
	s_waitcnt lgkmcnt(6)
	v_mfma_f32_16x16x32_bf16 v[12:15], v[164:167], v[68:71], v[12:15]
	v_exp_f32_e32 v86, v86
	v_exp_f32_e32 v87, v87
	v_add_f32_e32 v194, v194, v80
	v_mfma_f32_16x16x32_bf16 v[8:11], v[164:167], v[64:67], v[8:11]
	v_add_f32_e32 v194, v194, v81
	v_add_f32_e32 v194, v194, v82
	v_add_f32_e32 v194, v194, v83
	ds_read_b128 v[160:163], v210 offset:32768
	s_waitcnt lgkmcnt(6)
	v_mfma_f32_16x16x32_bf16 v[16:19], v[168:171], v[64:67], v[16:19]
	v_add_f32_e32 v195, v195, v84
	v_add_f32_e32 v195, v195, v85
	v_add_f32_e32 v195, v195, v86
	v_mfma_f32_16x16x32_bf16 v[20:23], v[168:171], v[68:71], v[20:23]
	v_add_f32_e32 v195, v195, v87
	v_cvt_pk_bf16_f32 v80, v80, v81
	v_cvt_pk_bf16_f32 v81, v82, v83
	ds_read_b128 v[164:167], v210 offset:34816
	s_waitcnt lgkmcnt(6)
	v_mfma_f32_16x16x32_bf16 v[28:31], v[172:175], v[68:71], v[28:31]
	v_cvt_pk_bf16_f32 v84, v84, v85
	v_cvt_pk_bf16_f32 v85, v86, v87
	v_mfma_f32_16x16x32_bf16 v[24:27], v[172:175], v[64:67], v[24:27]
	ds_read_b128 v[168:171], v210 offset:36864
	s_waitcnt lgkmcnt(6)
	v_mfma_f32_16x16x32_bf16 v[32:35], v[176:179], v[64:67], v[32:35]
	v_exp_f32_e32 v88, v88
	v_exp_f32_e32 v89, v89
	v_exp_f32_e32 v90, v90
	v_mfma_f32_16x16x32_bf16 v[36:39], v[176:179], v[68:71], v[36:39]
	v_exp_f32_e32 v91, v91
	v_exp_f32_e32 v92, v92
	v_exp_f32_e32 v93, v93
	ds_read_b128 v[172:175], v210 offset:38912
	s_waitcnt lgkmcnt(6)
	v_mfma_f32_16x16x32_bf16 v[44:47], v[180:183], v[68:71], v[44:47]
	v_exp_f32_e32 v94, v94
	v_exp_f32_e32 v95, v95
	v_add_f32_e32 v194, v194, v88
	v_mfma_f32_16x16x32_bf16 v[40:43], v[180:183], v[64:67], v[40:43]
	v_add_f32_e32 v194, v194, v89
	v_add_f32_e32 v194, v194, v90
	v_add_f32_e32 v194, v194, v91
	ds_read_b128 v[176:179], v210 offset:40960
	s_waitcnt lgkmcnt(6)
	v_mfma_f32_16x16x32_bf16 v[48:51], v[230:233], v[64:67], v[48:51]
	v_add_f32_e32 v195, v195, v92
	v_add_f32_e32 v195, v195, v93
	v_add_f32_e32 v195, v195, v94
	v_mfma_f32_16x16x32_bf16 v[52:55], v[230:233], v[68:71], v[52:55]
	v_add_f32_e32 v195, v195, v95
	v_cvt_pk_bf16_f32 v82, v88, v89
	v_cvt_pk_bf16_f32 v83, v90, v91
	ds_read_b128 v[180:183], v210 offset:43008
	s_waitcnt lgkmcnt(6)
	v_mfma_f32_16x16x32_bf16 v[60:63], v[234:237], v[68:71], v[60:63]
	v_cvt_pk_bf16_f32 v86, v92, v93
	v_cvt_pk_bf16_f32 v87, v94, v95
	v_mfma_f32_16x16x32_bf16 v[56:59], v[234:237], v[64:67], v[56:59]
	ds_read_b128 v[230:233], v210 offset:45056
	s_waitcnt lgkmcnt(6)
	v_mfma_f32_16x16x32_bf16 v[0:3], v[160:163], v[80:83], v[0:3]
	v_mfma_f32_16x16x32_bf16 v[4:7], v[160:163], v[84:87], v[4:7]
	ds_read_b128 v[234:237], v210 offset:47104
	s_waitcnt lgkmcnt(6)
	v_mfma_f32_16x16x32_bf16 v[12:15], v[164:167], v[84:87], v[12:15]
	v_mfma_f32_16x16x32_bf16 v[8:11], v[164:167], v[80:83], v[8:11]
	ds_read_b128 v[160:163], v201 offset:49152
	s_waitcnt lgkmcnt(6)
	v_mfma_f32_16x16x32_bf16 v[16:19], v[168:171], v[80:83], v[16:19]
	v_mfma_f32_16x16x32_bf16 v[20:23], v[168:171], v[84:87], v[20:23]
	ds_read_b128 v[164:167], v202 offset:49152
	s_waitcnt lgkmcnt(6)
	v_mfma_f32_16x16x32_bf16 v[28:31], v[172:175], v[84:87], v[28:31]
	v_mfma_f32_16x16x32_bf16 v[24:27], v[172:175], v[80:83], v[24:27]
	ds_read_b128 v[168:171], v203 offset:49152
	s_waitcnt lgkmcnt(6)
	v_mfma_f32_16x16x32_bf16 v[32:35], v[176:179], v[80:83], v[32:35]
	v_mfma_f32_16x16x32_bf16 v[36:39], v[176:179], v[84:87], v[36:39]
	ds_read_b128 v[172:175], v204 offset:49152
	s_waitcnt lgkmcnt(6)
	v_mfma_f32_16x16x32_bf16 v[44:47], v[180:183], v[84:87], v[44:47]
	v_mfma_f32_16x16x32_bf16 v[40:43], v[180:183], v[80:83], v[40:43]
	ds_read_b128 v[176:179], v201 offset:53248
	s_waitcnt lgkmcnt(6)
	v_mfma_f32_16x16x32_bf16 v[48:51], v[230:233], v[80:83], v[48:51]
	v_mfma_f32_16x16x32_bf16 v[52:55], v[230:233], v[84:87], v[52:55]
	ds_read_b128 v[180:183], v202 offset:53248
	s_waitcnt lgkmcnt(6)
	v_mfma_f32_16x16x32_bf16 v[60:63], v[234:237], v[84:87], v[60:63]
	v_mfma_f32_16x16x32_bf16 v[56:59], v[234:237], v[80:83], v[56:59]
	ds_read_b128 v[230:233], v203 offset:53248
	s_waitcnt lgkmcnt(6)
	v_mfma_f32_16x16x32_bf16 v[64:67], v[160:163], v[96:99], 0
	v_mfma_f32_16x16x32_bf16 v[68:71], v[160:163], v[112:115], 0
	ds_read_b128 v[234:237], v204 offset:53248
	s_add_u32 s8, s16, 0x3bc00380
	s_addc_u32 s9, s17, 0
	s_add_u32 s6, s15, 0x23a70000
	s_addc_u32 s7, s14, 0
	s_waitcnt lgkmcnt(6)
	v_mfma_f32_16x16x32_bf16 v[68:71], v[164:167], v[116:119], v[68:71]
	v_mfma_f32_16x16x32_bf16 v[64:67], v[164:167], v[100:103], v[64:67]
	ds_read_b128 v[160:163], v201 offset:57344
	s_waitcnt vmcnt(4)
	ds_write_b128 v225, v[152:155] offset:16384
	s_waitcnt lgkmcnt(7)
	v_mfma_f32_16x16x32_bf16 v[64:67], v[168:171], v[104:107], v[64:67]
	v_mfma_f32_16x16x32_bf16 v[68:71], v[168:171], v[120:123], v[68:71]
	ds_read_b128 v[164:167], v202 offset:57344
	ds_write_b128 v226, v[156:159] offset:16384
	s_waitcnt lgkmcnt(8)
	v_mfma_f32_16x16x32_bf16 v[68:71], v[172:175], v[124:127], v[68:71]
	v_mfma_f32_16x16x32_bf16 v[64:67], v[172:175], v[108:111], v[64:67]
	ds_read_b128 v[168:171], v203 offset:57344
	ds_write_b64 v227, v[148:149] offset:16384
	s_waitcnt lgkmcnt(9)
	v_mfma_f32_16x16x32_bf16 v[72:75], v[176:179], v[96:99], 0
	v_mfma_f32_16x16x32_bf16 v[76:79], v[176:179], v[112:115], 0
	ds_read_b128 v[172:175], v204 offset:57344
	ds_write_b64 v228, v[150:151] offset:16384
	s_waitcnt lgkmcnt(10)
	v_mfma_f32_16x16x32_bf16 v[76:79], v[180:183], v[116:119], v[76:79]
	v_mfma_f32_16x16x32_bf16 v[72:75], v[180:183], v[100:103], v[72:75]
	ds_read_b128 v[176:179], v201 offset:61440
	ds_write_b64 v229, v[144:145] offset:16384
	s_waitcnt lgkmcnt(11)
	v_mfma_f32_16x16x32_bf16 v[72:75], v[230:233], v[104:107], v[72:75]
	v_mfma_f32_16x16x32_bf16 v[76:79], v[230:233], v[120:123], v[76:79]
	ds_read_b128 v[180:183], v202 offset:61440
	ds_write_b64 v184, v[146:147] offset:16384
	s_waitcnt lgkmcnt(12)
	v_mfma_f32_16x16x32_bf16 v[76:79], v[234:237], v[124:127], v[76:79]
	v_mfma_f32_16x16x32_bf16 v[72:75], v[234:237], v[108:111], v[72:75]
	ds_read_b128 v[230:233], v203 offset:61440
	global_load_dwordx4 v[148:151], v198, s[8:9]
	s_waitcnt lgkmcnt(12)
	v_mfma_f32_16x16x32_bf16 v[80:83], v[160:163], v[96:99], 0
	v_exp_f32_e32 v64, v64
	v_exp_f32_e32 v65, v65
	v_exp_f32_e32 v66, v66
	v_mfma_f32_16x16x32_bf16 v[84:87], v[160:163], v[112:115], 0
	v_exp_f32_e32 v67, v67
	v_exp_f32_e32 v68, v68
	v_exp_f32_e32 v69, v69
	ds_read_b128 v[234:237], v204 offset:61440
	global_load_dwordx4 v[144:147], v199, s[8:9]
	s_waitcnt lgkmcnt(11)
	v_mfma_f32_16x16x32_bf16 v[84:87], v[164:167], v[116:119], v[84:87]
	v_exp_f32_e32 v70, v70
	v_exp_f32_e32 v71, v71
	v_add_f32_e32 v194, v194, v64
	v_mfma_f32_16x16x32_bf16 v[80:83], v[164:167], v[100:103], v[80:83]
	v_add_f32_e32 v194, v194, v65
	v_add_f32_e32 v194, v194, v66
	v_add_f32_e32 v194, v194, v67
	ds_read_b128 v[160:163], v209 offset:49152
	global_load_dwordx4 v[152:155], v196, s[6:7]
	s_waitcnt lgkmcnt(10)
	v_mfma_f32_16x16x32_bf16 v[80:83], v[168:171], v[104:107], v[80:83]
	v_add_f32_e32 v195, v195, v68
	v_add_f32_e32 v195, v195, v69
	v_add_f32_e32 v195, v195, v70
	v_mfma_f32_16x16x32_bf16 v[84:87], v[168:171], v[120:123], v[84:87]
	v_add_f32_e32 v195, v195, v71
	v_cvt_pk_bf16_f32 v64, v64, v65
	v_cvt_pk_bf16_f32 v65, v66, v67
	ds_read_b128 v[164:167], v209 offset:51200
	global_load_dwordx4 v[156:159], v197, s[6:7]
	s_waitcnt lgkmcnt(9)
	v_mfma_f32_16x16x32_bf16 v[84:87], v[172:175], v[124:127], v[84:87]
	v_cvt_pk_bf16_f32 v68, v68, v69
	v_cvt_pk_bf16_f32 v69, v70, v71
	v_mfma_f32_16x16x32_bf16 v[80:83], v[172:175], v[108:111], v[80:83]
	ds_read_b128 v[168:171], v209 offset:53248
	s_waitcnt lgkmcnt(8)
	v_mfma_f32_16x16x32_bf16 v[88:91], v[176:179], v[96:99], 0
	v_exp_f32_e32 v72, v72
	v_exp_f32_e32 v73, v73
	v_exp_f32_e32 v74, v74
	v_mfma_f32_16x16x32_bf16 v[92:95], v[176:179], v[112:115], 0
	v_exp_f32_e32 v75, v75
	v_exp_f32_e32 v76, v76
	v_exp_f32_e32 v77, v77
	ds_read_b128 v[172:175], v209 offset:55296
	s_waitcnt lgkmcnt(7)
	v_mfma_f32_16x16x32_bf16 v[92:95], v[180:183], v[116:119], v[92:95]
	v_exp_f32_e32 v78, v78
	v_exp_f32_e32 v79, v79
	v_add_f32_e32 v194, v194, v72
	v_mfma_f32_16x16x32_bf16 v[88:91], v[180:183], v[100:103], v[88:91]
	v_add_f32_e32 v194, v194, v73
	v_add_f32_e32 v194, v194, v74
	v_add_f32_e32 v194, v194, v75
	ds_read_b128 v[176:179], v209 offset:57344
	s_waitcnt lgkmcnt(6)
	v_mfma_f32_16x16x32_bf16 v[88:91], v[230:233], v[104:107], v[88:91]
	v_add_f32_e32 v195, v195, v76
	v_add_f32_e32 v195, v195, v77
	v_add_f32_e32 v195, v195, v78
	v_mfma_f32_16x16x32_bf16 v[92:95], v[230:233], v[120:123], v[92:95]
	v_add_f32_e32 v195, v195, v79
	v_cvt_pk_bf16_f32 v66, v72, v73
	v_cvt_pk_bf16_f32 v67, v74, v75
	ds_read_b128 v[180:183], v209 offset:59392
	s_waitcnt lgkmcnt(6)
	v_mfma_f32_16x16x32_bf16 v[92:95], v[234:237], v[124:127], v[92:95]
	v_cvt_pk_bf16_f32 v70, v76, v77
	v_cvt_pk_bf16_f32 v71, v78, v79
	v_mfma_f32_16x16x32_bf16 v[88:91], v[234:237], v[108:111], v[88:91]
	ds_read_b128 v[230:233], v209 offset:61440
	s_waitcnt lgkmcnt(6)
	v_mfma_f32_16x16x32_bf16 v[0:3], v[160:163], v[64:67], v[0:3]
	v_exp_f32_e32 v80, v80
	v_exp_f32_e32 v81, v81
	v_exp_f32_e32 v82, v82
	v_mfma_f32_16x16x32_bf16 v[4:7], v[160:163], v[68:71], v[4:7]
	v_exp_f32_e32 v83, v83
	v_exp_f32_e32 v84, v84
	v_exp_f32_e32 v85, v85
	ds_read_b128 v[234:237], v209 offset:63488
	s_waitcnt lgkmcnt(6)
	v_mfma_f32_16x16x32_bf16 v[12:15], v[164:167], v[68:71], v[12:15]
	v_exp_f32_e32 v86, v86
	v_exp_f32_e32 v87, v87
	v_add_f32_e32 v194, v194, v80
	v_mfma_f32_16x16x32_bf16 v[8:11], v[164:167], v[64:67], v[8:11]
	v_add_f32_e32 v194, v194, v81
	v_add_f32_e32 v194, v194, v82
	v_add_f32_e32 v194, v194, v83
	ds_read_b128 v[160:163], v210 offset:49152
	s_waitcnt lgkmcnt(6)
	v_mfma_f32_16x16x32_bf16 v[16:19], v[168:171], v[64:67], v[16:19]
	v_add_f32_e32 v195, v195, v84
	v_add_f32_e32 v195, v195, v85
	v_add_f32_e32 v195, v195, v86
	v_mfma_f32_16x16x32_bf16 v[20:23], v[168:171], v[68:71], v[20:23]
	v_add_f32_e32 v195, v195, v87
	v_cvt_pk_bf16_f32 v80, v80, v81
	v_cvt_pk_bf16_f32 v81, v82, v83
	ds_read_b128 v[164:167], v210 offset:51200
	s_waitcnt lgkmcnt(6)
	v_mfma_f32_16x16x32_bf16 v[28:31], v[172:175], v[68:71], v[28:31]
	v_cvt_pk_bf16_f32 v84, v84, v85
	v_cvt_pk_bf16_f32 v85, v86, v87
	v_mfma_f32_16x16x32_bf16 v[24:27], v[172:175], v[64:67], v[24:27]
	ds_read_b128 v[168:171], v210 offset:53248
	s_waitcnt lgkmcnt(6)
	v_mfma_f32_16x16x32_bf16 v[32:35], v[176:179], v[64:67], v[32:35]
	v_exp_f32_e32 v88, v88
	v_exp_f32_e32 v89, v89
	v_exp_f32_e32 v90, v90
	v_mfma_f32_16x16x32_bf16 v[36:39], v[176:179], v[68:71], v[36:39]
	v_exp_f32_e32 v91, v91
	v_exp_f32_e32 v92, v92
	v_exp_f32_e32 v93, v93
	ds_read_b128 v[172:175], v210 offset:55296
	s_add_u32 s10, s10, 0x200
	s_addc_u32 s11, s11, 0
	s_add_u32 s12, s12, 0x40000
	s_addc_u32 s13, s13, 0
	s_add_i32 s4, s4, 4
	s_cmpk_lt_u32 s4, 0x104
	s_cselect_b64 s[6:7], -1, 0
	s_and_b64 s[6:7], s[0:1], s[6:7]
	s_and_b64 vcc, exec, s[6:7]
	s_waitcnt lgkmcnt(6)
	v_mfma_f32_16x16x32_bf16 v[44:47], v[180:183], v[68:71], v[44:47]
	v_exp_f32_e32 v94, v94
	v_exp_f32_e32 v95, v95
	v_add_f32_e32 v194, v194, v88
	v_mfma_f32_16x16x32_bf16 v[40:43], v[180:183], v[64:67], v[40:43]
	v_add_f32_e32 v194, v194, v89
	v_add_f32_e32 v194, v194, v90
	v_add_f32_e32 v194, v194, v91
	ds_read_b128 v[176:179], v210 offset:57344
	s_waitcnt lgkmcnt(6)
	v_mfma_f32_16x16x32_bf16 v[48:51], v[230:233], v[64:67], v[48:51]
	v_add_f32_e32 v195, v195, v92
	v_add_f32_e32 v195, v195, v93
	v_add_f32_e32 v195, v195, v94
	v_mfma_f32_16x16x32_bf16 v[52:55], v[230:233], v[68:71], v[52:55]
	v_add_f32_e32 v195, v195, v95
	v_cvt_pk_bf16_f32 v82, v88, v89
	v_cvt_pk_bf16_f32 v83, v90, v91
	ds_read_b128 v[180:183], v210 offset:59392
	s_waitcnt lgkmcnt(6)
	v_mfma_f32_16x16x32_bf16 v[60:63], v[234:237], v[68:71], v[60:63]
	v_cvt_pk_bf16_f32 v86, v92, v93
	v_cvt_pk_bf16_f32 v87, v94, v95
	v_mfma_f32_16x16x32_bf16 v[56:59], v[234:237], v[64:67], v[56:59]
	ds_read_b128 v[230:233], v210 offset:61440
	s_waitcnt lgkmcnt(6)
	v_mfma_f32_16x16x32_bf16 v[0:3], v[160:163], v[80:83], v[0:3]
	v_mfma_f32_16x16x32_bf16 v[4:7], v[160:163], v[84:87], v[4:7]
	ds_read_b128 v[234:237], v210 offset:63488
	s_waitcnt lgkmcnt(6)
	v_mfma_f32_16x16x32_bf16 v[12:15], v[164:167], v[84:87], v[12:15]
	v_mfma_f32_16x16x32_bf16 v[8:11], v[164:167], v[80:83], v[8:11]
	s_waitcnt lgkmcnt(5)
	v_mfma_f32_16x16x32_bf16 v[16:19], v[168:171], v[80:83], v[16:19]
	v_mfma_f32_16x16x32_bf16 v[20:23], v[168:171], v[84:87], v[20:23]
	s_waitcnt lgkmcnt(4)
	v_mfma_f32_16x16x32_bf16 v[28:31], v[172:175], v[84:87], v[28:31]
	v_mfma_f32_16x16x32_bf16 v[24:27], v[172:175], v[80:83], v[24:27]
	s_waitcnt lgkmcnt(3)
	v_mfma_f32_16x16x32_bf16 v[32:35], v[176:179], v[80:83], v[32:35]
	v_mfma_f32_16x16x32_bf16 v[36:39], v[176:179], v[84:87], v[36:39]
	s_waitcnt lgkmcnt(2)
	v_mfma_f32_16x16x32_bf16 v[44:47], v[180:183], v[84:87], v[44:47]
	v_mfma_f32_16x16x32_bf16 v[40:43], v[180:183], v[80:83], v[40:43]
	s_waitcnt lgkmcnt(1)
	v_mfma_f32_16x16x32_bf16 v[48:51], v[230:233], v[80:83], v[48:51]
	v_mfma_f32_16x16x32_bf16 v[52:55], v[230:233], v[84:87], v[52:55]
	s_waitcnt lgkmcnt(0)
	v_mfma_f32_16x16x32_bf16 v[60:63], v[234:237], v[84:87], v[60:63]
	v_mfma_f32_16x16x32_bf16 v[56:59], v[234:237], v[80:83], v[56:59]
	s_cbranch_vccnz .LBB0_734
	s_waitcnt vmcnt(0)
	s_nop 7
	s_nop 7
	ds_swizzle_b32 v64, v194 offset:swizzle(SWAP,16)
	s_waitcnt lgkmcnt(0)
	v_add_f32_e32 v194, v194, v64
	v_mov_b32_e32 v65, v194
	s_nop 1
	v_permlane32_swap_b32_e32 v194, v65
	v_add_f32_e32 v194, v194, v65
	s_nop 0
	v_rcp_f32_e32 v66, v194
	ds_swizzle_b32 v64, v195 offset:swizzle(SWAP,16)
	s_waitcnt lgkmcnt(0)
	v_add_f32_e32 v195, v195, v64
	v_mov_b32_e32 v65, v195
	s_nop 1
	v_permlane32_swap_b32_e32 v195, v65
	v_add_f32_e32 v195, v195, v65
	s_nop 0
	v_rcp_f32_e32 v67, v195
	v_readlane_b32 s100, v250, 8
	v_mbcnt_lo_u32_b32 v68, -1, 0
	v_mbcnt_hi_u32_b32 v68, -1, v68
	v_and_b32_e32 v69, 15, v68
	v_lshrrev_b32_e32 v70, 4, v68
	s_lshr_b32 s101, s100, 1
	v_add_u32_e32 v69, s101, v69
	v_lshlrev_b32_e32 v69, 12, v69
	v_and_b32_e32 v71, 1, v70
	v_lshlrev_b32_e32 v71, 5, v71
	v_and_b32_e32 v70, 2, v70
	v_lshl_add_u32 v71, v70, 3, v71
	v_add_u32_e32 v70, v69, v71
	v_add_u32_e32 v71, 0x10000, v70
	v_mul_f32_e32 v0, v0, v66
	v_mul_f32_e32 v1, v1, v66
	v_mul_f32_e32 v2, v2, v66
	v_mul_f32_e32 v3, v3, v66
	v_mul_f32_e32 v8, v8, v66
	v_mul_f32_e32 v9, v9, v66
	v_mul_f32_e32 v10, v10, v66
	v_mul_f32_e32 v11, v11, v66
	v_cvt_pk_bf16_f32 v72, v0, v1
	v_cvt_pk_bf16_f32 v73, v2, v3
	v_cvt_pk_bf16_f32 v74, v8, v9
	v_cvt_pk_bf16_f32 v75, v10, v11
	s_nop 1
	v_permlane16_swap_b32_e32 v72, v74
	v_permlane16_swap_b32_e32 v73, v75
	s_nop 1
	global_store_dwordx4 v70, v[72:75], s[58:59] offset:0
	v_mul_f32_e32 v16, v16, v66
	v_mul_f32_e32 v17, v17, v66
	v_mul_f32_e32 v18, v18, v66
	v_mul_f32_e32 v19, v19, v66
	v_mul_f32_e32 v24, v24, v66
	v_mul_f32_e32 v25, v25, v66
	v_mul_f32_e32 v26, v26, v66
	v_mul_f32_e32 v27, v27, v66
	v_cvt_pk_bf16_f32 v76, v16, v17
	v_cvt_pk_bf16_f32 v77, v18, v19
	v_cvt_pk_bf16_f32 v78, v24, v25
	v_cvt_pk_bf16_f32 v79, v26, v27
	s_nop 1
	v_permlane16_swap_b32_e32 v76, v78
	v_permlane16_swap_b32_e32 v77, v79
	s_nop 1
	global_store_dwordx4 v70, v[76:79], s[58:59] offset:64
	v_mul_f32_e32 v32, v32, v66
	v_mul_f32_e32 v33, v33, v66
	v_mul_f32_e32 v34, v34, v66
	v_mul_f32_e32 v35, v35, v66
	v_mul_f32_e32 v40, v40, v66
	v_mul_f32_e32 v41, v41, v66
	v_mul_f32_e32 v42, v42, v66
	v_mul_f32_e32 v43, v43, v66
	v_cvt_pk_bf16_f32 v80, v32, v33
	v_cvt_pk_bf16_f32 v81, v34, v35
	v_cvt_pk_bf16_f32 v82, v40, v41
	v_cvt_pk_bf16_f32 v83, v42, v43
	s_nop 1
	v_permlane16_swap_b32_e32 v80, v82
	v_permlane16_swap_b32_e32 v81, v83
	s_nop 1
	global_store_dwordx4 v70, v[80:83], s[58:59] offset:128
	v_mul_f32_e32 v48, v48, v66
	v_mul_f32_e32 v49, v49, v66
	v_mul_f32_e32 v50, v50, v66
	v_mul_f32_e32 v51, v51, v66
	v_mul_f32_e32 v56, v56, v66
	v_mul_f32_e32 v57, v57, v66
	v_mul_f32_e32 v58, v58, v66
	v_mul_f32_e32 v59, v59, v66
	v_cvt_pk_bf16_f32 v84, v48, v49
	v_cvt_pk_bf16_f32 v85, v50, v51
	v_cvt_pk_bf16_f32 v86, v56, v57
	v_cvt_pk_bf16_f32 v87, v58, v59
	s_nop 1
	v_permlane16_swap_b32_e32 v84, v86
	v_permlane16_swap_b32_e32 v85, v87
	s_nop 1
	global_store_dwordx4 v70, v[84:87], s[58:59] offset:192
	v_mul_f32_e32 v4, v4, v67
	v_mul_f32_e32 v5, v5, v67
	v_mul_f32_e32 v6, v6, v67
	v_mul_f32_e32 v7, v7, v67
	v_mul_f32_e32 v12, v12, v67
	v_mul_f32_e32 v13, v13, v67
	v_mul_f32_e32 v14, v14, v67
	v_mul_f32_e32 v15, v15, v67
	v_cvt_pk_bf16_f32 v88, v4, v5
	v_cvt_pk_bf16_f32 v89, v6, v7
	v_cvt_pk_bf16_f32 v90, v12, v13
	v_cvt_pk_bf16_f32 v91, v14, v15
	s_nop 1
	v_permlane16_swap_b32_e32 v88, v90
	v_permlane16_swap_b32_e32 v89, v91
	s_nop 1
	global_store_dwordx4 v71, v[88:91], s[58:59] offset:0
	v_mul_f32_e32 v20, v20, v67
	v_mul_f32_e32 v21, v21, v67
	v_mul_f32_e32 v22, v22, v67
	v_mul_f32_e32 v23, v23, v67
	v_mul_f32_e32 v28, v28, v67
	v_mul_f32_e32 v29, v29, v67
	v_mul_f32_e32 v30, v30, v67
	v_mul_f32_e32 v31, v31, v67
	v_cvt_pk_bf16_f32 v92, v20, v21
	v_cvt_pk_bf16_f32 v93, v22, v23
	v_cvt_pk_bf16_f32 v94, v28, v29
	v_cvt_pk_bf16_f32 v95, v30, v31
	s_nop 1
	v_permlane16_swap_b32_e32 v92, v94
	v_permlane16_swap_b32_e32 v93, v95
	s_nop 1
	global_store_dwordx4 v71, v[92:95], s[58:59] offset:64
	v_mul_f32_e32 v36, v36, v67
	v_mul_f32_e32 v37, v37, v67
	v_mul_f32_e32 v38, v38, v67
	v_mul_f32_e32 v39, v39, v67
	v_mul_f32_e32 v44, v44, v67
	v_mul_f32_e32 v45, v45, v67
	v_mul_f32_e32 v46, v46, v67
	v_mul_f32_e32 v47, v47, v67
	v_cvt_pk_bf16_f32 v72, v36, v37
	v_cvt_pk_bf16_f32 v73, v38, v39
	v_cvt_pk_bf16_f32 v74, v44, v45
	v_cvt_pk_bf16_f32 v75, v46, v47
	s_nop 1
	v_permlane16_swap_b32_e32 v72, v74
	v_permlane16_swap_b32_e32 v73, v75
	s_nop 1
	global_store_dwordx4 v71, v[72:75], s[58:59] offset:128
	v_mul_f32_e32 v52, v52, v67
	v_mul_f32_e32 v53, v53, v67
	v_mul_f32_e32 v54, v54, v67
	v_mul_f32_e32 v55, v55, v67
	v_mul_f32_e32 v60, v60, v67
	v_mul_f32_e32 v61, v61, v67
	v_mul_f32_e32 v62, v62, v67
	v_mul_f32_e32 v63, v63, v67
	v_cvt_pk_bf16_f32 v76, v52, v53
	v_cvt_pk_bf16_f32 v77, v54, v55
	v_cvt_pk_bf16_f32 v78, v60, v61
	v_cvt_pk_bf16_f32 v79, v62, v63
	s_nop 1
	v_permlane16_swap_b32_e32 v76, v78
	v_permlane16_swap_b32_e32 v77, v79
	s_nop 1
	global_store_dwordx4 v71, v[76:79], s[58:59] offset:192
	s_barrier
